# k_f3 + removed the two compiler-inserted s_waitcnt vmcnt(0) at the top of the q-up / kv-up K-loops (restores counted-wait DMA pipelining)
# baseline (speedup 1.0000x reference)
;     __device__ __forceinline__ bool next(int i, Unit& u) const { return so.next(i, u); }
; #define PG8_STAGE(bufoff, gbase, voff) do { _Pragma("unroll") for (int _i = 0; _i < 2; ++_i) \
;         __builtin_amdgcn_global_load_lds((const unsigned*)((const char*)(gbase) + (voff)[_i]), (PG8_LAS unsigned*)(lds + (bufoff) + ldsw + _i * 8192), 16, 0, 0); } while (0)
; #define PG8_WAIT_V(n) asm volatile("s_waitcnt vmcnt(" #n ")" ::: "memory")
; #define PG8_WAIT_L(n) asm volatile("s_waitcnt lgkmcnt(" #n ")" ::: "memory")
; #define PG8_BAR __builtin_amdgcn_s_barrier()
; #define PG8_SCHED __builtin_amdgcn_sched_barrier(0)
; template <class Epi, class Sched, bool ALIGN_EPI = false, bool SP2 = false, bool F8 = false>
; __device__ __forceinline__ void gemm_phase(PG8_LAS unsigned char* lds, const Gemm g, const Sched& S, const Epi& E, const int tidb  ) {
;     ...
;         const bool has_next = S.next(ui + 1, nxt);
;         const char* nA = has_next ? (const char*)g.A + (size_t)nxt.pm * tstep : cA; const char* nB = has_next ? (const char*)g.Bt + S.boff(nxt) + (size_t)nxt.pn * tstep : cB;
;         for (int t = 0; t < nt; t += 2) {
;             const bool last = (t == nt - 2);
;             if constexpr (Epi::PREFETCH) { if (t == 0) E.prefetch(cur, wid, lane); }
;             const char* a1 = cA + (size_t)(t + 1) * kstep;
;             const char* a2 = last ? nA : cA + (size_t)(t + 2) * kstep; const char* b2 = last ? nB : cB + (size_t)(t + 2) * kstep;
;             const char* a3 = a2 + kstep; const char* b3 = b2 + kstep;
;             if (last && has_next) S.a_ready(nxt);
;             if constexpr (SP2) {
;             PG8_LDB(B0, 0, 0); PG8_LDB(B1, 0, 1); PG8_SCHED; PG8_LDA(At, 0, 0); PG8_STAGE(PG8_SA(1, 1), a1 + hstep, voffA);
;             PG8_WAIT_V(8); PG8_WAIT_L(0); PG8_BAR; PG8_MMA(0, 0, At, B0); PG8_MMA(0, 1, At, B1); PG8_BAR; PG8_SCHED;
;             PG8_LDA(At, 0, 1); PG8_STAGE(PG8_SB(0, 0), b2, voffB); PG8_STAGE(PG8_SB(0, 1), b2 + hstep, voffB); PG8_STAGE(PG8_SA(0, 0), a2, voffA);
;             PG8_WAIT_V(8); PG8_WAIT_L(0); PG8_BAR; PG8_MMA(1, 0, At, B0); PG8_MMA(1, 1, At, B1); PG8_BAR; PG8_SCHED;
.LBB0_393:
	s_add_i32 s63, s28, 2
	s_add_u32 s65, s4, 0x80
	s_addc_u32 s29, s5, 0
	s_add_i32 s68, 0, 0x10000
	s_cmp_eq_u32 s55, s28
	s_cselect_b32 s29, s25, s29
	s_cselect_b32 s28, s24, s65
	v_add_u32_e32 v0, s68, v152
	s_cselect_b32 s67, s27, s31
	s_cselect_b32 s66, s26, s30
	s_add_i32 s65, 0, 0x14000
	ds_read_b128 v[158:161], v0
	ds_read_b128 v[164:167], v0 offset:1024
	ds_read_b128 v[168:171], v0 offset:2048
	ds_read_b128 v[172:175], v0 offset:3072
	v_add_u32_e32 v0, s65, v152
	ds_read_b128 v[176:179], v0
	ds_read_b128 v[180:183], v0 offset:1024
	ds_read_b128 v[184:187], v0 offset:2048
	ds_read_b128 v[188:191], v0 offset:3072
	v_lshl_add_u64 v[148:149], s[4:5], 0, v[144:145]
	s_add_i32 m0, s46, 0xc000
	ds_read_b128 v[192:195], v156
	ds_read_b128 v[204:207], v156 offset:1024
	ds_read_b128 v[208:211], v156 offset:2048
	ds_read_b128 v[212:215], v156 offset:3072
	ds_read_b128 v[216:219], v156 offset:4096
	ds_read_b128 v[220:223], v156 offset:5120
	ds_read_b128 v[224:227], v156 offset:6144
	ds_read_b128 v[228:231], v156 offset:7168
	global_load_lds_dwordx4 v[148:149], off
	v_lshl_add_u64 v[148:149], s[4:5], 0, v[146:147]
	s_add_i32 m0, s46, 0xe000
	s_nop 0
	global_load_lds_dwordx4 v[148:149], off
	s_waitcnt vmcnt(8)
	s_waitcnt lgkmcnt(0)
	s_barrier
	s_setprio 1
	s_waitcnt lgkmcnt(0)
	v_mfma_f32_16x16x32_bf16 v[122:125], v[158:161], v[192:195], v[122:125]
	v_mfma_f32_16x16x32_bf16 v[126:129], v[168:171], v[192:195], v[126:129]
	v_mfma_f32_16x16x32_bf16 v[118:121], v[158:161], v[208:211], v[118:121]
	v_mfma_f32_16x16x32_bf16 v[114:117], v[168:171], v[208:211], v[114:117]
	v_mfma_f32_16x16x32_bf16 v[110:113], v[158:161], v[216:219], v[110:113]
	v_mfma_f32_16x16x32_bf16 v[106:109], v[168:171], v[216:219], v[106:109]
	v_mfma_f32_16x16x32_bf16 v[102:105], v[158:161], v[224:227], v[102:105]
	v_mfma_f32_16x16x32_bf16 v[98:101], v[168:171], v[224:227], v[98:101]
	v_mfma_f32_16x16x32_bf16 v[122:125], v[164:167], v[204:207], v[122:125]
	v_mfma_f32_16x16x32_bf16 v[126:129], v[172:175], v[204:207], v[126:129]
	v_mfma_f32_16x16x32_bf16 v[118:121], v[164:167], v[212:215], v[118:121]
	v_mfma_f32_16x16x32_bf16 v[114:117], v[172:175], v[212:215], v[114:117]
	v_mfma_f32_16x16x32_bf16 v[110:113], v[164:167], v[220:223], v[110:113]
	v_mfma_f32_16x16x32_bf16 v[106:109], v[172:175], v[220:223], v[106:109]
	v_mfma_f32_16x16x32_bf16 v[102:105], v[164:167], v[228:231], v[102:105]
	v_mfma_f32_16x16x32_bf16 v[98:101], v[172:175], v[228:231], v[98:101]
	s_setprio 0
	s_setprio 1
	v_mfma_f32_16x16x32_bf16 v[62:65], v[176:179], v[192:195], v[62:65]
	v_mfma_f32_16x16x32_bf16 v[58:61], v[184:187], v[192:195], v[58:61]
	v_mfma_f32_16x16x32_bf16 v[54:57], v[176:179], v[208:211], v[54:57]
	v_mfma_f32_16x16x32_bf16 v[50:53], v[184:187], v[208:211], v[50:53]
	v_mfma_f32_16x16x32_bf16 v[46:49], v[176:179], v[216:219], v[46:49]
	v_mfma_f32_16x16x32_bf16 v[42:45], v[184:187], v[216:219], v[42:45]
	v_mfma_f32_16x16x32_bf16 v[38:41], v[176:179], v[224:227], v[38:41]
	v_mfma_f32_16x16x32_bf16 v[34:37], v[184:187], v[224:227], v[34:37]
	v_mfma_f32_16x16x32_bf16 v[62:65], v[180:183], v[204:207], v[62:65]
	v_mfma_f32_16x16x32_bf16 v[58:61], v[188:191], v[204:207], v[58:61]
	v_mfma_f32_16x16x32_bf16 v[54:57], v[180:183], v[212:215], v[54:57]
	v_mfma_f32_16x16x32_bf16 v[50:53], v[188:191], v[212:215], v[50:53]
	v_mfma_f32_16x16x32_bf16 v[46:49], v[180:183], v[220:223], v[46:49]
	v_mfma_f32_16x16x32_bf16 v[42:45], v[188:191], v[220:223], v[42:45]
	v_mfma_f32_16x16x32_bf16 v[38:41], v[180:183], v[228:231], v[38:41]
	v_mfma_f32_16x16x32_bf16 v[34:37], v[188:191], v[228:231], v[34:37]
	s_setprio 0
	s_barrier
	s_add_i32 s68, s68, s45
	v_lshl_add_u64 v[148:149], s[66:67], 0, v[132:133]
	s_mov_b32 m0, s68
	ds_read_b128 v[192:195], v156 offset:16384
	ds_read_b128 v[204:207], v156 offset:17408
	ds_read_b128 v[208:211], v156 offset:18432
	ds_read_b128 v[212:215], v156 offset:19456
	ds_read_b128 v[216:219], v156 offset:20480
	ds_read_b128 v[220:223], v156 offset:21504
	ds_read_b128 v[224:227], v156 offset:22528
	ds_read_b128 v[228:231], v156 offset:23552
	global_load_lds_dwordx4 v[148:149], off
	s_add_i32 m0, s68, 0x2000
	v_lshl_add_u64 v[196:197], s[66:67], 0, v[136:137]
	s_add_u32 s66, s66, s10
	s_addc_u32 s67, s67, s11
	s_add_i32 s65, s65, s45
	global_load_lds_dwordx4 v[196:197], off
	v_lshl_add_u64 v[200:201], s[66:67], 0, v[132:133]
	s_mov_b32 m0, s65
	v_lshl_add_u64 v[232:233], s[66:67], 0, v[136:137]
	global_load_lds_dwordx4 v[200:201], off
	s_add_i32 m0, s65, 0x2000
	v_lshl_add_u64 v[234:235], s[28:29], 0, v[130:131]
	global_load_lds_dwordx4 v[232:233], off
	s_mov_b32 m0, s46
	v_lshl_add_u64 v[236:237], s[28:29], 0, v[134:135]
	global_load_lds_dwordx4 v[234:235], off
	s_mov_b32 m0, s47
	s_nop 0
	global_load_lds_dwordx4 v[236:237], off
	s_waitcnt vmcnt(8)
	s_waitcnt lgkmcnt(0)
	s_barrier
; #define PG8_STAGE(bufoff, gbase, voff) do { _Pragma("unroll") for (int _i = 0; _i < 2; ++_i) \
;         __builtin_amdgcn_global_load_lds((const unsigned*)((const char*)(gbase) + (voff)[_i]), (PG8_LAS unsigned*)(lds + (bufoff) + ldsw + _i * 8192), 16, 0, 0); } while (0)
; #define PG8_WAIT_V(n) asm volatile("s_waitcnt vmcnt(" #n ")" ::: "memory")
; #define PG8_WAIT_L(n) asm volatile("s_waitcnt lgkmcnt(" #n ")" ::: "memory")
; #define PG8_BAR __builtin_amdgcn_s_barrier()
; #define PG8_SCHED __builtin_amdgcn_sched_barrier(0)
; template <class Epi, class Sched, bool ALIGN_EPI = false, bool SP2 = false, bool F8 = false>
; __device__ __forceinline__ void gemm_phase(PG8_LAS unsigned char* lds, const Gemm g, const Sched& S, const Epi& E, const int tidb  ) {
;     ...
;             PG8_WAIT_V(8); PG8_WAIT_L(0); PG8_BAR; PG8_MMA(1, 0, At, B0); PG8_MMA(1, 1, At, B1); PG8_BAR; PG8_SCHED;
;             PG8_LDB(B0, 1, 0); PG8_LDB(B1, 1, 1); PG8_SCHED; PG8_LDA(At, 1, 0); PG8_STAGE(PG8_SA(0, 1), a2 + hstep, voffA);
;             PG8_WAIT_V(8); PG8_WAIT_L(0); PG8_BAR; PG8_MMA(0, 0, At, B0); PG8_MMA(0, 1, At, B1); PG8_BAR; PG8_SCHED;
	s_setprio 1
	s_waitcnt lgkmcnt(0)
	v_mfma_f32_16x16x32_bf16 v[94:97], v[158:161], v[192:195], v[94:97]
	v_mfma_f32_16x16x32_bf16 v[90:93], v[168:171], v[192:195], v[90:93]
	v_mfma_f32_16x16x32_bf16 v[86:89], v[158:161], v[208:211], v[86:89]
	v_mfma_f32_16x16x32_bf16 v[82:85], v[168:171], v[208:211], v[82:85]
	v_mfma_f32_16x16x32_bf16 v[78:81], v[158:161], v[216:219], v[78:81]
	v_mfma_f32_16x16x32_bf16 v[74:77], v[168:171], v[216:219], v[74:77]
	v_mfma_f32_16x16x32_bf16 v[70:73], v[158:161], v[224:227], v[70:73]
	v_mfma_f32_16x16x32_bf16 v[66:69], v[168:171], v[224:227], v[66:69]
	v_mfma_f32_16x16x32_bf16 v[94:97], v[164:167], v[204:207], v[94:97]
	v_mfma_f32_16x16x32_bf16 v[90:93], v[172:175], v[204:207], v[90:93]
	v_mfma_f32_16x16x32_bf16 v[86:89], v[164:167], v[212:215], v[86:89]
	v_mfma_f32_16x16x32_bf16 v[82:85], v[172:175], v[212:215], v[82:85]
	v_mfma_f32_16x16x32_bf16 v[78:81], v[164:167], v[220:223], v[78:81]
	v_mfma_f32_16x16x32_bf16 v[74:77], v[172:175], v[220:223], v[74:77]
	v_mfma_f32_16x16x32_bf16 v[70:73], v[164:167], v[228:231], v[70:73]
	v_mfma_f32_16x16x32_bf16 v[66:69], v[172:175], v[228:231], v[66:69]
	s_setprio 0
	s_setprio 1
	v_mfma_f32_16x16x32_bf16 v[30:33], v[176:179], v[192:195], v[30:33]
	v_mfma_f32_16x16x32_bf16 v[26:29], v[184:187], v[192:195], v[26:29]
	v_mfma_f32_16x16x32_bf16 v[22:25], v[176:179], v[208:211], v[22:25]
	v_mfma_f32_16x16x32_bf16 v[18:21], v[184:187], v[208:211], v[18:21]
	v_mfma_f32_16x16x32_bf16 v[14:17], v[176:179], v[216:219], v[14:17]
	v_mfma_f32_16x16x32_bf16 v[10:13], v[184:187], v[216:219], v[10:13]
	v_mfma_f32_16x16x32_bf16 v[6:9], v[176:179], v[224:227], v[6:9]
	v_mfma_f32_16x16x32_bf16 v[2:5], v[184:187], v[224:227], v[2:5]
	v_mfma_f32_16x16x32_bf16 v[30:33], v[180:183], v[204:207], v[30:33]
	v_mfma_f32_16x16x32_bf16 v[26:29], v[188:191], v[204:207], v[26:29]
	v_mfma_f32_16x16x32_bf16 v[22:25], v[180:183], v[212:215], v[22:25]
	v_mfma_f32_16x16x32_bf16 v[18:21], v[188:191], v[212:215], v[18:21]
	v_mfma_f32_16x16x32_bf16 v[14:17], v[180:183], v[220:223], v[14:17]
	v_mfma_f32_16x16x32_bf16 v[10:13], v[188:191], v[220:223], v[10:13]
	v_mfma_f32_16x16x32_bf16 v[6:9], v[180:183], v[228:231], v[6:9]
	v_mfma_f32_16x16x32_bf16 v[2:5], v[188:191], v[228:231], v[2:5]
	s_setprio 0
	s_barrier
	s_add_i32 s65, 0, 0x18000
	v_add_u32_e32 v0, s65, v152
	s_add_i32 s66, 0, 0x1c000
	ds_read_b128 v[158:161], v0
	ds_read_b128 v[164:167], v0 offset:1024
	ds_read_b128 v[168:171], v0 offset:2048
	ds_read_b128 v[172:175], v0 offset:3072
	v_add_u32_e32 v0, s66, v152
	ds_read_b128 v[176:179], v0
	ds_read_b128 v[180:183], v0 offset:1024
	ds_read_b128 v[184:187], v0 offset:2048
	ds_read_b128 v[188:191], v0 offset:3072
	s_add_u32 s28, s28, s10
	s_addc_u32 s29, s29, s11
	s_mov_b32 m0, s48
	v_lshl_add_u64 v[238:239], s[28:29], 0, v[130:131]
	ds_read_b128 v[192:195], v156 offset:32768
	ds_read_b128 v[204:207], v156 offset:33792
	ds_read_b128 v[208:211], v156 offset:34816
	ds_read_b128 v[212:215], v156 offset:35840
	ds_read_b128 v[216:219], v156 offset:36864
	ds_read_b128 v[220:223], v156 offset:37888
	ds_read_b128 v[224:227], v156 offset:38912
	ds_read_b128 v[228:231], v156 offset:39936
	global_load_lds_dwordx4 v[238:239], off
	v_lshl_add_u64 v[238:239], s[28:29], 0, v[134:135]
	s_mov_b32 m0, s49
	s_nop 0
	global_load_lds_dwordx4 v[238:239], off
	s_waitcnt vmcnt(8)
	s_waitcnt lgkmcnt(0)
	s_barrier
	s_setprio 1
	s_waitcnt lgkmcnt(0)
	v_mfma_f32_16x16x32_bf16 v[122:125], v[158:161], v[192:195], v[122:125]
	v_mfma_f32_16x16x32_bf16 v[126:129], v[168:171], v[192:195], v[126:129]
	v_mfma_f32_16x16x32_bf16 v[118:121], v[158:161], v[208:211], v[118:121]
	v_mfma_f32_16x16x32_bf16 v[114:117], v[168:171], v[208:211], v[114:117]
	v_mfma_f32_16x16x32_bf16 v[110:113], v[158:161], v[216:219], v[110:113]
	v_mfma_f32_16x16x32_bf16 v[106:109], v[168:171], v[216:219], v[106:109]
	v_mfma_f32_16x16x32_bf16 v[102:105], v[158:161], v[224:227], v[102:105]
	v_mfma_f32_16x16x32_bf16 v[98:101], v[168:171], v[224:227], v[98:101]
	v_mfma_f32_16x16x32_bf16 v[122:125], v[164:167], v[204:207], v[122:125]
	v_mfma_f32_16x16x32_bf16 v[126:129], v[172:175], v[204:207], v[126:129]
	v_mfma_f32_16x16x32_bf16 v[118:121], v[164:167], v[212:215], v[118:121]
	v_mfma_f32_16x16x32_bf16 v[114:117], v[172:175], v[212:215], v[114:117]
	v_mfma_f32_16x16x32_bf16 v[110:113], v[164:167], v[220:223], v[110:113]
	v_mfma_f32_16x16x32_bf16 v[106:109], v[172:175], v[220:223], v[106:109]
	v_mfma_f32_16x16x32_bf16 v[102:105], v[164:167], v[228:231], v[102:105]
	v_mfma_f32_16x16x32_bf16 v[98:101], v[172:175], v[228:231], v[98:101]
	s_setprio 0
	s_setprio 1
	v_mfma_f32_16x16x32_bf16 v[62:65], v[176:179], v[192:195], v[62:65]
	v_mfma_f32_16x16x32_bf16 v[58:61], v[184:187], v[192:195], v[58:61]
	v_mfma_f32_16x16x32_bf16 v[54:57], v[176:179], v[208:211], v[54:57]
	v_mfma_f32_16x16x32_bf16 v[50:53], v[184:187], v[208:211], v[50:53]
	v_mfma_f32_16x16x32_bf16 v[46:49], v[176:179], v[216:219], v[46:49]
	v_mfma_f32_16x16x32_bf16 v[42:45], v[184:187], v[216:219], v[42:45]
	v_mfma_f32_16x16x32_bf16 v[38:41], v[176:179], v[224:227], v[38:41]
	v_mfma_f32_16x16x32_bf16 v[34:37], v[184:187], v[224:227], v[34:37]
	v_mfma_f32_16x16x32_bf16 v[62:65], v[180:183], v[204:207], v[62:65]
	v_mfma_f32_16x16x32_bf16 v[58:61], v[188:191], v[204:207], v[58:61]
	v_mfma_f32_16x16x32_bf16 v[54:57], v[180:183], v[212:215], v[54:57]
	v_mfma_f32_16x16x32_bf16 v[50:53], v[188:191], v[212:215], v[50:53]
	v_mfma_f32_16x16x32_bf16 v[46:49], v[180:183], v[220:223], v[46:49]
	v_mfma_f32_16x16x32_bf16 v[42:45], v[188:191], v[220:223], v[42:45]
	v_mfma_f32_16x16x32_bf16 v[38:41], v[180:183], v[228:231], v[38:41]
	v_mfma_f32_16x16x32_bf16 v[34:37], v[188:191], v[228:231], v[34:37]
	s_setprio 0
	s_barrier
; #define PG8_STAGE(bufoff, gbase, voff) do { _Pragma("unroll") for (int _i = 0; _i < 2; ++_i) \
;         __builtin_amdgcn_global_load_lds((const unsigned*)((const char*)(gbase) + (voff)[_i]), (PG8_LAS unsigned*)(lds + (bufoff) + ldsw + _i * 8192), 16, 0, 0); } while (0)
; #define PG8_WAIT_V(n) asm volatile("s_waitcnt vmcnt(" #n ")" ::: "memory")
; #define PG8_WAIT_L(n) asm volatile("s_waitcnt lgkmcnt(" #n ")" ::: "memory")
; #define PG8_BAR __builtin_amdgcn_s_barrier()
; #define PG8_SCHED __builtin_amdgcn_sched_barrier(0)
; template <class Epi, class Sched, bool ALIGN_EPI = false, bool SP2 = false, bool F8 = false>
; __device__ __forceinline__ void gemm_phase(PG8_LAS unsigned char* lds, const Gemm g, const Sched& S, const Epi& E, const int tidb  ) {
;     ...
;         for (int t = 0; t < nt; t += 2) {
;             const bool last = (t == nt - 2);
;             if constexpr (Epi::PREFETCH) { if (t == 0) E.prefetch(cur, wid, lane); }
;             const char* a1 = cA + (size_t)(t + 1) * kstep;
;             const char* a2 = last ? nA : cA + (size_t)(t + 2) * kstep; const char* b2 = last ? nB : cB + (size_t)(t + 2) * kstep;
;             const char* a3 = a2 + kstep; const char* b3 = b2 + kstep;
;     ...
;             PG8_LDA(At, 1, 1); PG8_STAGE(PG8_SB(1, 0), b3, voffB); PG8_STAGE(PG8_SB(1, 1), b3 + hstep, voffB); PG8_STAGE(PG8_SA(1, 0), a3, voffA);
;             PG8_WAIT_V(8); PG8_WAIT_L(0); PG8_BAR; PG8_MMA(1, 0, At, B0); PG8_MMA(1, 1, At, B1); PG8_BAR; PG8_SCHED;
	s_add_i32 s28, s65, s45
	v_lshl_add_u64 v[148:149], v[148:149], 0, s[92:93]
	s_mov_b32 m0, s28
	ds_read_b128 v[192:195], v156 offset:49152
	ds_read_b128 v[204:207], v156 offset:50176
	ds_read_b128 v[208:211], v156 offset:51200
	ds_read_b128 v[212:215], v156 offset:52224
	ds_read_b128 v[216:219], v156 offset:53248
	ds_read_b128 v[220:223], v156 offset:54272
	ds_read_b128 v[224:227], v156 offset:55296
	ds_read_b128 v[228:231], v156 offset:56320
	global_load_lds_dwordx4 v[148:149], off
	v_lshl_add_u64 v[148:149], v[196:197], 0, s[92:93]
	s_add_i32 m0, s28, 0x2000
	s_add_i32 s28, s66, s45
	global_load_lds_dwordx4 v[148:149], off
	v_lshl_add_u64 v[148:149], v[200:201], 0, s[92:93]
	s_mov_b32 m0, s28
	s_nop 0
	global_load_lds_dwordx4 v[148:149], off
	v_lshl_add_u64 v[148:149], v[232:233], 0, s[92:93]
	s_add_i32 m0, s28, 0x2000
	s_nop 0
	global_load_lds_dwordx4 v[148:149], off
	v_lshl_add_u64 v[148:149], v[234:235], 0, s[92:93]
	s_mov_b32 m0, s50
	s_nop 0
	global_load_lds_dwordx4 v[148:149], off
	v_lshl_add_u64 v[148:149], v[236:237], 0, s[92:93]
	s_mov_b32 m0, s51
	s_nop 0
	global_load_lds_dwordx4 v[148:149], off
	s_waitcnt vmcnt(8)
	s_waitcnt lgkmcnt(0)
	s_barrier
	s_setprio 1
	s_waitcnt lgkmcnt(0)
	v_mfma_f32_16x16x32_bf16 v[94:97], v[158:161], v[192:195], v[94:97]
	v_mfma_f32_16x16x32_bf16 v[90:93], v[168:171], v[192:195], v[90:93]
	v_mfma_f32_16x16x32_bf16 v[86:89], v[158:161], v[208:211], v[86:89]
	v_mfma_f32_16x16x32_bf16 v[82:85], v[168:171], v[208:211], v[82:85]
	v_mfma_f32_16x16x32_bf16 v[78:81], v[158:161], v[216:219], v[78:81]
	v_mfma_f32_16x16x32_bf16 v[74:77], v[168:171], v[216:219], v[74:77]
	v_mfma_f32_16x16x32_bf16 v[70:73], v[158:161], v[224:227], v[70:73]
	v_mfma_f32_16x16x32_bf16 v[66:69], v[168:171], v[224:227], v[66:69]
	v_mfma_f32_16x16x32_bf16 v[94:97], v[164:167], v[204:207], v[94:97]
	v_mfma_f32_16x16x32_bf16 v[90:93], v[172:175], v[204:207], v[90:93]
	v_mfma_f32_16x16x32_bf16 v[86:89], v[164:167], v[212:215], v[86:89]
	v_mfma_f32_16x16x32_bf16 v[82:85], v[172:175], v[212:215], v[82:85]
	v_mfma_f32_16x16x32_bf16 v[78:81], v[164:167], v[220:223], v[78:81]
	v_mfma_f32_16x16x32_bf16 v[74:77], v[172:175], v[220:223], v[74:77]
	v_mfma_f32_16x16x32_bf16 v[70:73], v[164:167], v[228:231], v[70:73]
	v_mfma_f32_16x16x32_bf16 v[66:69], v[172:175], v[228:231], v[66:69]
	s_setprio 0
	s_setprio 1
	v_mfma_f32_16x16x32_bf16 v[30:33], v[176:179], v[192:195], v[30:33]
	v_mfma_f32_16x16x32_bf16 v[26:29], v[184:187], v[192:195], v[26:29]
	v_mfma_f32_16x16x32_bf16 v[22:25], v[176:179], v[208:211], v[22:25]
	v_mfma_f32_16x16x32_bf16 v[18:21], v[184:187], v[208:211], v[18:21]
	v_mfma_f32_16x16x32_bf16 v[14:17], v[176:179], v[216:219], v[14:17]
	v_mfma_f32_16x16x32_bf16 v[10:13], v[184:187], v[216:219], v[10:13]
	v_mfma_f32_16x16x32_bf16 v[6:9], v[176:179], v[224:227], v[6:9]
	v_mfma_f32_16x16x32_bf16 v[2:5], v[184:187], v[224:227], v[2:5]
	v_mfma_f32_16x16x32_bf16 v[30:33], v[180:183], v[204:207], v[30:33]
	v_mfma_f32_16x16x32_bf16 v[26:29], v[188:191], v[204:207], v[26:29]
	v_mfma_f32_16x16x32_bf16 v[22:25], v[180:183], v[212:215], v[22:25]
	v_mfma_f32_16x16x32_bf16 v[18:21], v[188:191], v[212:215], v[18:21]
	v_mfma_f32_16x16x32_bf16 v[14:17], v[180:183], v[220:223], v[14:17]
	v_mfma_f32_16x16x32_bf16 v[10:13], v[188:191], v[220:223], v[10:13]
	v_mfma_f32_16x16x32_bf16 v[6:9], v[180:183], v[228:231], v[6:9]
	v_mfma_f32_16x16x32_bf16 v[2:5], v[188:191], v[228:231], v[2:5]
	s_setprio 0
	s_add_u32 s4, s4, 0x100
	s_addc_u32 s5, s5, 0
	s_add_u32 s30, s30, 0x100
	s_addc_u32 s31, s31, 0
	s_cmp_ge_i32 s63, s52
	s_mov_b32 s28, s63
	s_barrier
	s_cbranch_scc0 .LBB0_393
	s_movk_i32 s67, 0x300

;     __device__ __forceinline__ bool next(int i, Unit& u) const { return so.next(i, u); }
; #define PG8_STAGE(bufoff, gbase, voff) do { _Pragma("unroll") for (int _i = 0; _i < 2; ++_i) \
;         __builtin_amdgcn_global_load_lds((const unsigned*)((const char*)(gbase) + (voff)[_i]), (PG8_LAS unsigned*)(lds + (bufoff) + ldsw + _i * 8192), 16, 0, 0); } while (0)
; #define PG8_WAIT_V(n) asm volatile("s_waitcnt vmcnt(" #n ")" ::: "memory")
; #define PG8_WAIT_L(n) asm volatile("s_waitcnt lgkmcnt(" #n ")" ::: "memory")
; #define PG8_BAR __builtin_amdgcn_s_barrier()
; #define PG8_SCHED __builtin_amdgcn_sched_barrier(0)
; template <class Epi, class Sched, bool ALIGN_EPI = false, bool SP2 = false, bool F8 = false>
; __device__ __forceinline__ void gemm_phase(PG8_LAS unsigned char* lds, const Gemm g, const Sched& S, const Epi& E, const int tidb  ) {
;     ...
;         const bool has_next = S.next(ui + 1, nxt);
;         const char* nA = has_next ? (const char*)g.A + (size_t)nxt.pm * tstep : cA; const char* nB = has_next ? (const char*)g.Bt + S.boff(nxt) + (size_t)nxt.pn * tstep : cB;
;         for (int t = 0; t < nt; t += 2) {
;             const bool last = (t == nt - 2);
;             if constexpr (Epi::PREFETCH) { if (t == 0) E.prefetch(cur, wid, lane); }
;             const char* a1 = cA + (size_t)(t + 1) * kstep;
;             const char* a2 = last ? nA : cA + (size_t)(t + 2) * kstep; const char* b2 = last ? nB : cB + (size_t)(t + 2) * kstep;
;             const char* a3 = a2 + kstep; const char* b3 = b2 + kstep;
;             if (last && has_next) S.a_ready(nxt);
;             if constexpr (SP2) {
;             PG8_LDB(B0, 0, 0); PG8_LDB(B1, 0, 1); PG8_SCHED; PG8_LDA(At, 0, 0); PG8_STAGE(PG8_SA(1, 1), a1 + hstep, voffA);
;             PG8_WAIT_V(8); PG8_WAIT_L(0); PG8_BAR; PG8_MMA(0, 0, At, B0); PG8_MMA(0, 1, At, B1); PG8_BAR; PG8_SCHED;
;             PG8_LDA(At, 0, 1); PG8_STAGE(PG8_SB(0, 0), b2, voffB); PG8_STAGE(PG8_SB(0, 1), b2 + hstep, voffB); PG8_STAGE(PG8_SA(0, 0), a2, voffA);
;             PG8_WAIT_V(8); PG8_WAIT_L(0); PG8_BAR; PG8_MMA(1, 0, At, B0); PG8_MMA(1, 1, At, B1); PG8_BAR; PG8_SCHED;
.LBB0_465:
	s_add_i32 s61, s6, 2
	s_add_u32 s62, s4, 0x80
	s_addc_u32 s7, s5, 0
	s_add_i32 s65, 0, 0x10000
	s_cmp_eq_u32 s54, s6
	s_cselect_b32 s7, s25, s7
	s_cselect_b32 s6, s24, s62
	v_add_u32_e32 v0, s65, v159
	s_cselect_b32 s63, s27, s29
	s_cselect_b32 s62, s26, s28
	s_add_i32 s66, 0, 0x14000
	ds_read_b128 v[142:145], v0
	ds_read_b128 v[146:149], v0 offset:1024
	ds_read_b128 v[154:157], v0 offset:2048
	ds_read_b128 v[164:167], v0 offset:3072
	v_add_u32_e32 v0, s66, v159
	ds_read_b128 v[168:171], v0
	ds_read_b128 v[172:175], v0 offset:1024
	ds_read_b128 v[176:179], v0 offset:2048
	ds_read_b128 v[180:183], v0 offset:3072
	v_lshl_add_u64 v[150:151], s[4:5], 0, v[138:139]
	s_add_i32 m0, s45, 0xc000
	ds_read_b128 v[184:187], v160
	ds_read_b128 v[188:191], v160 offset:1024
	ds_read_b128 v[192:195], v160 offset:2048
	ds_read_b128 v[204:207], v160 offset:3072
	ds_read_b128 v[208:211], v160 offset:4096
	ds_read_b128 v[212:215], v160 offset:5120
	ds_read_b128 v[216:219], v160 offset:6144
	ds_read_b128 v[220:223], v160 offset:7168
	global_load_lds_dwordx4 v[150:151], off
	v_lshl_add_u64 v[150:151], s[4:5], 0, v[140:141]
	s_add_i32 m0, s45, 0xe000
	s_nop 0
	global_load_lds_dwordx4 v[150:151], off
	s_waitcnt vmcnt(8)
	s_waitcnt lgkmcnt(0)
	s_barrier
	s_setprio 1
	s_waitcnt lgkmcnt(0)
	v_mfma_f32_16x16x32_bf16 v[126:129], v[142:145], v[184:187], v[126:129]
	v_mfma_f32_16x16x32_bf16 v[122:125], v[154:157], v[184:187], v[122:125]
	v_mfma_f32_16x16x32_bf16 v[118:121], v[142:145], v[192:195], v[118:121]
	v_mfma_f32_16x16x32_bf16 v[114:117], v[154:157], v[192:195], v[114:117]
	v_mfma_f32_16x16x32_bf16 v[110:113], v[142:145], v[208:211], v[110:113]
	v_mfma_f32_16x16x32_bf16 v[106:109], v[154:157], v[208:211], v[106:109]
	v_mfma_f32_16x16x32_bf16 v[102:105], v[142:145], v[216:219], v[102:105]
	v_mfma_f32_16x16x32_bf16 v[98:101], v[154:157], v[216:219], v[98:101]
	v_mfma_f32_16x16x32_bf16 v[126:129], v[146:149], v[188:191], v[126:129]
	v_mfma_f32_16x16x32_bf16 v[122:125], v[164:167], v[188:191], v[122:125]
	v_mfma_f32_16x16x32_bf16 v[118:121], v[146:149], v[204:207], v[118:121]
	v_mfma_f32_16x16x32_bf16 v[114:117], v[164:167], v[204:207], v[114:117]
	v_mfma_f32_16x16x32_bf16 v[110:113], v[146:149], v[212:215], v[110:113]
	v_mfma_f32_16x16x32_bf16 v[106:109], v[164:167], v[212:215], v[106:109]
	v_mfma_f32_16x16x32_bf16 v[102:105], v[146:149], v[220:223], v[102:105]
	v_mfma_f32_16x16x32_bf16 v[98:101], v[164:167], v[220:223], v[98:101]
	s_setprio 0
	s_setprio 1
	v_mfma_f32_16x16x32_bf16 v[62:65], v[168:171], v[184:187], v[62:65]
	v_mfma_f32_16x16x32_bf16 v[58:61], v[176:179], v[184:187], v[58:61]
	v_mfma_f32_16x16x32_bf16 v[54:57], v[168:171], v[192:195], v[54:57]
	v_mfma_f32_16x16x32_bf16 v[50:53], v[176:179], v[192:195], v[50:53]
	v_mfma_f32_16x16x32_bf16 v[46:49], v[168:171], v[208:211], v[46:49]
	v_mfma_f32_16x16x32_bf16 v[42:45], v[176:179], v[208:211], v[42:45]
	v_mfma_f32_16x16x32_bf16 v[38:41], v[168:171], v[216:219], v[38:41]
	v_mfma_f32_16x16x32_bf16 v[34:37], v[176:179], v[216:219], v[34:37]
	v_mfma_f32_16x16x32_bf16 v[62:65], v[172:175], v[188:191], v[62:65]
	v_mfma_f32_16x16x32_bf16 v[58:61], v[180:183], v[188:191], v[58:61]
	v_mfma_f32_16x16x32_bf16 v[54:57], v[172:175], v[204:207], v[54:57]
	v_mfma_f32_16x16x32_bf16 v[50:53], v[180:183], v[204:207], v[50:53]
	v_mfma_f32_16x16x32_bf16 v[46:49], v[172:175], v[212:215], v[46:49]
	v_mfma_f32_16x16x32_bf16 v[42:45], v[180:183], v[212:215], v[42:45]
	v_mfma_f32_16x16x32_bf16 v[38:41], v[172:175], v[220:223], v[38:41]
	v_mfma_f32_16x16x32_bf16 v[34:37], v[180:183], v[220:223], v[34:37]
	s_setprio 0
	s_barrier
	s_add_i32 s65, s65, s43
	v_lshl_add_u64 v[150:151], s[62:63], 0, v[132:133]
	s_mov_b32 m0, s65
	ds_read_b128 v[184:187], v160 offset:16384
	ds_read_b128 v[188:191], v160 offset:17408
	ds_read_b128 v[192:195], v160 offset:18432
	ds_read_b128 v[204:207], v160 offset:19456
	ds_read_b128 v[208:211], v160 offset:20480
	ds_read_b128 v[212:215], v160 offset:21504
	ds_read_b128 v[216:219], v160 offset:22528
	ds_read_b128 v[220:223], v160 offset:23552
	global_load_lds_dwordx4 v[150:151], off
	s_add_i32 m0, s65, 0x2000
	v_lshl_add_u64 v[196:197], s[62:63], 0, v[136:137]
	s_add_u32 s62, s62, s8
	s_addc_u32 s63, s63, s9
	s_add_i32 s65, s66, s43
	global_load_lds_dwordx4 v[196:197], off
	v_lshl_add_u64 v[200:201], s[62:63], 0, v[132:133]
	s_mov_b32 m0, s65
	v_lshl_add_u64 v[224:225], s[62:63], 0, v[136:137]
	global_load_lds_dwordx4 v[200:201], off
	s_add_i32 m0, s65, 0x2000
	v_lshl_add_u64 v[226:227], s[6:7], 0, v[130:131]
	global_load_lds_dwordx4 v[224:225], off
	s_mov_b32 m0, s45
	v_lshl_add_u64 v[228:229], s[6:7], 0, v[134:135]
	global_load_lds_dwordx4 v[226:227], off
	s_mov_b32 m0, s46
	s_nop 0
	global_load_lds_dwordx4 v[228:229], off
	s_waitcnt vmcnt(8)
	s_waitcnt lgkmcnt(0)
	s_barrier
; #define PG8_STAGE(bufoff, gbase, voff) do { _Pragma("unroll") for (int _i = 0; _i < 2; ++_i) \
;         __builtin_amdgcn_global_load_lds((const unsigned*)((const char*)(gbase) + (voff)[_i]), (PG8_LAS unsigned*)(lds + (bufoff) + ldsw + _i * 8192), 16, 0, 0); } while (0)
; #define PG8_WAIT_V(n) asm volatile("s_waitcnt vmcnt(" #n ")" ::: "memory")
; #define PG8_WAIT_L(n) asm volatile("s_waitcnt lgkmcnt(" #n ")" ::: "memory")
; #define PG8_BAR __builtin_amdgcn_s_barrier()
; #define PG8_SCHED __builtin_amdgcn_sched_barrier(0)
; template <class Epi, class Sched, bool ALIGN_EPI = false, bool SP2 = false, bool F8 = false>
; __device__ __forceinline__ void gemm_phase(PG8_LAS unsigned char* lds, const Gemm g, const Sched& S, const Epi& E, const int tidb  ) {
;     ...
;             PG8_WAIT_V(8); PG8_WAIT_L(0); PG8_BAR; PG8_MMA(1, 0, At, B0); PG8_MMA(1, 1, At, B1); PG8_BAR; PG8_SCHED;
;             PG8_LDB(B0, 1, 0); PG8_LDB(B1, 1, 1); PG8_SCHED; PG8_LDA(At, 1, 0); PG8_STAGE(PG8_SA(0, 1), a2 + hstep, voffA);
;             PG8_WAIT_V(8); PG8_WAIT_L(0); PG8_BAR; PG8_MMA(0, 0, At, B0); PG8_MMA(0, 1, At, B1); PG8_BAR; PG8_SCHED;
	s_setprio 1
	s_waitcnt lgkmcnt(0)
	v_mfma_f32_16x16x32_bf16 v[94:97], v[142:145], v[184:187], v[94:97]
	v_mfma_f32_16x16x32_bf16 v[90:93], v[154:157], v[184:187], v[90:93]
	v_mfma_f32_16x16x32_bf16 v[86:89], v[142:145], v[192:195], v[86:89]
	v_mfma_f32_16x16x32_bf16 v[82:85], v[154:157], v[192:195], v[82:85]
	v_mfma_f32_16x16x32_bf16 v[78:81], v[142:145], v[208:211], v[78:81]
	v_mfma_f32_16x16x32_bf16 v[74:77], v[154:157], v[208:211], v[74:77]
	v_mfma_f32_16x16x32_bf16 v[70:73], v[142:145], v[216:219], v[70:73]
	v_mfma_f32_16x16x32_bf16 v[66:69], v[154:157], v[216:219], v[66:69]
	v_mfma_f32_16x16x32_bf16 v[94:97], v[146:149], v[188:191], v[94:97]
	v_mfma_f32_16x16x32_bf16 v[90:93], v[164:167], v[188:191], v[90:93]
	v_mfma_f32_16x16x32_bf16 v[86:89], v[146:149], v[204:207], v[86:89]
	v_mfma_f32_16x16x32_bf16 v[82:85], v[164:167], v[204:207], v[82:85]
	v_mfma_f32_16x16x32_bf16 v[78:81], v[146:149], v[212:215], v[78:81]
	v_mfma_f32_16x16x32_bf16 v[74:77], v[164:167], v[212:215], v[74:77]
	v_mfma_f32_16x16x32_bf16 v[70:73], v[146:149], v[220:223], v[70:73]
	v_mfma_f32_16x16x32_bf16 v[66:69], v[164:167], v[220:223], v[66:69]
	s_setprio 0
	s_setprio 1
	v_mfma_f32_16x16x32_bf16 v[30:33], v[168:171], v[184:187], v[30:33]
	v_mfma_f32_16x16x32_bf16 v[26:29], v[176:179], v[184:187], v[26:29]
	v_mfma_f32_16x16x32_bf16 v[22:25], v[168:171], v[192:195], v[22:25]
	v_mfma_f32_16x16x32_bf16 v[18:21], v[176:179], v[192:195], v[18:21]
	v_mfma_f32_16x16x32_bf16 v[14:17], v[168:171], v[208:211], v[14:17]
	v_mfma_f32_16x16x32_bf16 v[10:13], v[176:179], v[208:211], v[10:13]
	v_mfma_f32_16x16x32_bf16 v[6:9], v[168:171], v[216:219], v[6:9]
	v_mfma_f32_16x16x32_bf16 v[2:5], v[176:179], v[216:219], v[2:5]
	v_mfma_f32_16x16x32_bf16 v[30:33], v[172:175], v[188:191], v[30:33]
	v_mfma_f32_16x16x32_bf16 v[26:29], v[180:183], v[188:191], v[26:29]
	v_mfma_f32_16x16x32_bf16 v[22:25], v[172:175], v[204:207], v[22:25]
	v_mfma_f32_16x16x32_bf16 v[18:21], v[180:183], v[204:207], v[18:21]
	v_mfma_f32_16x16x32_bf16 v[14:17], v[172:175], v[212:215], v[14:17]
	v_mfma_f32_16x16x32_bf16 v[10:13], v[180:183], v[212:215], v[10:13]
	v_mfma_f32_16x16x32_bf16 v[6:9], v[172:175], v[220:223], v[6:9]
	v_mfma_f32_16x16x32_bf16 v[2:5], v[180:183], v[220:223], v[2:5]
	s_setprio 0
	s_barrier
	s_add_i32 s62, 0, 0x18000
	v_add_u32_e32 v0, s62, v159
	s_add_i32 s63, 0, 0x1c000
	ds_read_b128 v[142:145], v0
	ds_read_b128 v[146:149], v0 offset:1024
	ds_read_b128 v[154:157], v0 offset:2048
	ds_read_b128 v[164:167], v0 offset:3072
	v_add_u32_e32 v0, s63, v159
	ds_read_b128 v[168:171], v0
	ds_read_b128 v[172:175], v0 offset:1024
	ds_read_b128 v[176:179], v0 offset:2048
	ds_read_b128 v[180:183], v0 offset:3072
	s_add_u32 s6, s6, s8
	s_addc_u32 s7, s7, s9
	s_mov_b32 m0, s47
	v_lshl_add_u64 v[230:231], s[6:7], 0, v[130:131]
	ds_read_b128 v[184:187], v160 offset:32768
	ds_read_b128 v[188:191], v160 offset:33792
	ds_read_b128 v[192:195], v160 offset:34816
	ds_read_b128 v[204:207], v160 offset:35840
	ds_read_b128 v[208:211], v160 offset:36864
	ds_read_b128 v[212:215], v160 offset:37888
	ds_read_b128 v[216:219], v160 offset:38912
	ds_read_b128 v[220:223], v160 offset:39936
	global_load_lds_dwordx4 v[230:231], off
	v_lshl_add_u64 v[230:231], s[6:7], 0, v[134:135]
	s_mov_b32 m0, s48
	s_nop 0
	global_load_lds_dwordx4 v[230:231], off
	s_waitcnt vmcnt(8)
	s_waitcnt lgkmcnt(0)
	s_barrier
	s_setprio 1
	s_waitcnt lgkmcnt(0)
	v_mfma_f32_16x16x32_bf16 v[126:129], v[142:145], v[184:187], v[126:129]
	v_mfma_f32_16x16x32_bf16 v[122:125], v[154:157], v[184:187], v[122:125]
	v_mfma_f32_16x16x32_bf16 v[118:121], v[142:145], v[192:195], v[118:121]
	v_mfma_f32_16x16x32_bf16 v[114:117], v[154:157], v[192:195], v[114:117]
	v_mfma_f32_16x16x32_bf16 v[110:113], v[142:145], v[208:211], v[110:113]
	v_mfma_f32_16x16x32_bf16 v[106:109], v[154:157], v[208:211], v[106:109]
	v_mfma_f32_16x16x32_bf16 v[102:105], v[142:145], v[216:219], v[102:105]
	v_mfma_f32_16x16x32_bf16 v[98:101], v[154:157], v[216:219], v[98:101]
	v_mfma_f32_16x16x32_bf16 v[126:129], v[146:149], v[188:191], v[126:129]
	v_mfma_f32_16x16x32_bf16 v[122:125], v[164:167], v[188:191], v[122:125]
	v_mfma_f32_16x16x32_bf16 v[118:121], v[146:149], v[204:207], v[118:121]
	v_mfma_f32_16x16x32_bf16 v[114:117], v[164:167], v[204:207], v[114:117]
	v_mfma_f32_16x16x32_bf16 v[110:113], v[146:149], v[212:215], v[110:113]
	v_mfma_f32_16x16x32_bf16 v[106:109], v[164:167], v[212:215], v[106:109]
	v_mfma_f32_16x16x32_bf16 v[102:105], v[146:149], v[220:223], v[102:105]
	v_mfma_f32_16x16x32_bf16 v[98:101], v[164:167], v[220:223], v[98:101]
	s_setprio 0
	s_setprio 1
	v_mfma_f32_16x16x32_bf16 v[62:65], v[168:171], v[184:187], v[62:65]
	v_mfma_f32_16x16x32_bf16 v[58:61], v[176:179], v[184:187], v[58:61]
	v_mfma_f32_16x16x32_bf16 v[54:57], v[168:171], v[192:195], v[54:57]
	v_mfma_f32_16x16x32_bf16 v[50:53], v[176:179], v[192:195], v[50:53]
	v_mfma_f32_16x16x32_bf16 v[46:49], v[168:171], v[208:211], v[46:49]
	v_mfma_f32_16x16x32_bf16 v[42:45], v[176:179], v[208:211], v[42:45]
	v_mfma_f32_16x16x32_bf16 v[38:41], v[168:171], v[216:219], v[38:41]
	v_mfma_f32_16x16x32_bf16 v[34:37], v[176:179], v[216:219], v[34:37]
	v_mfma_f32_16x16x32_bf16 v[62:65], v[172:175], v[188:191], v[62:65]
	v_mfma_f32_16x16x32_bf16 v[58:61], v[180:183], v[188:191], v[58:61]
	v_mfma_f32_16x16x32_bf16 v[54:57], v[172:175], v[204:207], v[54:57]
	v_mfma_f32_16x16x32_bf16 v[50:53], v[180:183], v[204:207], v[50:53]
	v_mfma_f32_16x16x32_bf16 v[46:49], v[172:175], v[212:215], v[46:49]
	v_mfma_f32_16x16x32_bf16 v[42:45], v[180:183], v[212:215], v[42:45]
	v_mfma_f32_16x16x32_bf16 v[38:41], v[172:175], v[220:223], v[38:41]
	v_mfma_f32_16x16x32_bf16 v[34:37], v[180:183], v[220:223], v[34:37]
	s_setprio 0
	s_barrier
; #define PG8_STAGE(bufoff, gbase, voff) do { _Pragma("unroll") for (int _i = 0; _i < 2; ++_i) \
;         __builtin_amdgcn_global_load_lds((const unsigned*)((const char*)(gbase) + (voff)[_i]), (PG8_LAS unsigned*)(lds + (bufoff) + ldsw + _i * 8192), 16, 0, 0); } while (0)
; #define PG8_WAIT_V(n) asm volatile("s_waitcnt vmcnt(" #n ")" ::: "memory")
; #define PG8_WAIT_L(n) asm volatile("s_waitcnt lgkmcnt(" #n ")" ::: "memory")
; #define PG8_BAR __builtin_amdgcn_s_barrier()
; #define PG8_SCHED __builtin_amdgcn_sched_barrier(0)
; template <class Epi, class Sched, bool ALIGN_EPI = false, bool SP2 = false, bool F8 = false>
; __device__ __forceinline__ void gemm_phase(PG8_LAS unsigned char* lds, const Gemm g, const Sched& S, const Epi& E, const int tidb  ) {
;     ...
;             PG8_LDA(At, 1, 1); PG8_STAGE(PG8_SB(1, 0), b3, voffB); PG8_STAGE(PG8_SB(1, 1), b3 + hstep, voffB); PG8_STAGE(PG8_SA(1, 0), a3, voffA);
;             PG8_WAIT_V(8); PG8_WAIT_L(0); PG8_BAR; PG8_MMA(1, 0, At, B0); PG8_MMA(1, 1, At, B1); PG8_BAR; PG8_SCHED;
	s_add_i32 s6, s62, s43
	v_lshl_add_u64 v[150:151], v[150:151], 0, s[92:93]
	s_mov_b32 m0, s6
	ds_read_b128 v[184:187], v160 offset:49152
	ds_read_b128 v[188:191], v160 offset:50176
	ds_read_b128 v[192:195], v160 offset:51200
	ds_read_b128 v[204:207], v160 offset:52224
	ds_read_b128 v[208:211], v160 offset:53248
	ds_read_b128 v[212:215], v160 offset:54272
	ds_read_b128 v[216:219], v160 offset:55296
	ds_read_b128 v[220:223], v160 offset:56320
	global_load_lds_dwordx4 v[150:151], off
	v_lshl_add_u64 v[150:151], v[196:197], 0, s[92:93]
	s_add_i32 m0, s6, 0x2000
	s_add_i32 s6, s63, s43
	global_load_lds_dwordx4 v[150:151], off
	v_lshl_add_u64 v[150:151], v[200:201], 0, s[92:93]
	s_mov_b32 m0, s6
	s_nop 0
	global_load_lds_dwordx4 v[150:151], off
	v_lshl_add_u64 v[150:151], v[224:225], 0, s[92:93]
	s_add_i32 m0, s6, 0x2000
	s_nop 0
	global_load_lds_dwordx4 v[150:151], off
	v_lshl_add_u64 v[150:151], v[226:227], 0, s[92:93]
	s_mov_b32 m0, s49
	s_nop 0
	global_load_lds_dwordx4 v[150:151], off
	v_lshl_add_u64 v[150:151], v[228:229], 0, s[92:93]
	s_mov_b32 m0, s50
	s_nop 0
	global_load_lds_dwordx4 v[150:151], off
	s_waitcnt vmcnt(8)
	s_waitcnt lgkmcnt(0)
	s_barrier
	s_setprio 1
	s_waitcnt lgkmcnt(0)
	v_mfma_f32_16x16x32_bf16 v[94:97], v[142:145], v[184:187], v[94:97]
	v_mfma_f32_16x16x32_bf16 v[90:93], v[154:157], v[184:187], v[90:93]
	v_mfma_f32_16x16x32_bf16 v[86:89], v[142:145], v[192:195], v[86:89]
	v_mfma_f32_16x16x32_bf16 v[82:85], v[154:157], v[192:195], v[82:85]
	v_mfma_f32_16x16x32_bf16 v[78:81], v[142:145], v[208:211], v[78:81]
	v_mfma_f32_16x16x32_bf16 v[74:77], v[154:157], v[208:211], v[74:77]
	v_mfma_f32_16x16x32_bf16 v[70:73], v[142:145], v[216:219], v[70:73]
	v_mfma_f32_16x16x32_bf16 v[66:69], v[154:157], v[216:219], v[66:69]
	v_mfma_f32_16x16x32_bf16 v[94:97], v[146:149], v[188:191], v[94:97]
	v_mfma_f32_16x16x32_bf16 v[90:93], v[164:167], v[188:191], v[90:93]
	v_mfma_f32_16x16x32_bf16 v[86:89], v[146:149], v[204:207], v[86:89]
	v_mfma_f32_16x16x32_bf16 v[82:85], v[164:167], v[204:207], v[82:85]
	v_mfma_f32_16x16x32_bf16 v[78:81], v[146:149], v[212:215], v[78:81]
	v_mfma_f32_16x16x32_bf16 v[74:77], v[164:167], v[212:215], v[74:77]
	v_mfma_f32_16x16x32_bf16 v[70:73], v[146:149], v[220:223], v[70:73]
	v_mfma_f32_16x16x32_bf16 v[66:69], v[164:167], v[220:223], v[66:69]
	s_setprio 0
	s_setprio 1
	v_mfma_f32_16x16x32_bf16 v[30:33], v[168:171], v[184:187], v[30:33]
	v_mfma_f32_16x16x32_bf16 v[26:29], v[176:179], v[184:187], v[26:29]
	v_mfma_f32_16x16x32_bf16 v[22:25], v[168:171], v[192:195], v[22:25]
	v_mfma_f32_16x16x32_bf16 v[18:21], v[176:179], v[192:195], v[18:21]
	v_mfma_f32_16x16x32_bf16 v[14:17], v[168:171], v[208:211], v[14:17]
	v_mfma_f32_16x16x32_bf16 v[10:13], v[176:179], v[208:211], v[10:13]
	v_mfma_f32_16x16x32_bf16 v[6:9], v[168:171], v[216:219], v[6:9]
	v_mfma_f32_16x16x32_bf16 v[2:5], v[176:179], v[216:219], v[2:5]
	v_mfma_f32_16x16x32_bf16 v[30:33], v[172:175], v[188:191], v[30:33]
	v_mfma_f32_16x16x32_bf16 v[26:29], v[180:183], v[188:191], v[26:29]
	v_mfma_f32_16x16x32_bf16 v[22:25], v[172:175], v[204:207], v[22:25]
	v_mfma_f32_16x16x32_bf16 v[18:21], v[180:183], v[204:207], v[18:21]
	v_mfma_f32_16x16x32_bf16 v[14:17], v[172:175], v[212:215], v[14:17]
	v_mfma_f32_16x16x32_bf16 v[10:13], v[180:183], v[212:215], v[10:13]
	v_mfma_f32_16x16x32_bf16 v[6:9], v[172:175], v[220:223], v[6:9]
	v_mfma_f32_16x16x32_bf16 v[2:5], v[180:183], v[220:223], v[2:5]
	s_setprio 0
	s_add_u32 s4, s4, 0x100
	s_addc_u32 s5, s5, 0
	s_add_u32 s28, s28, 0x100
	s_addc_u32 s29, s29, 0
	s_cmp_ge_i32 s61, s51
	s_mov_b32 s6, s61
	s_barrier
	s_cbranch_scc0 .LBB0_465
